# v5 + grid barrier steady-state path rewritten compactly (same two-level protocol: per-XCD counter, L2 write-back, returning cross-XCD arrival, generation word; barrier number in s98 instead of two int
# speedup vs baseline: 1.0056x; 1.0036x over previous
; __device__ __forceinline__ int tid_from_wave(int wave) { unsigned l_; asm volatile("v_mbcnt_lo_u32_b32 %0, -1, 0\n\tv_mbcnt_hi_u32_b32 %0, -1, %0" : "=v"(l_)); return wave * 64 + (int)l_; }
; __device__ __forceinline__ unsigned xb_ld(unsigned* p)              { return __hip_atomic_load(p, __ATOMIC_RELAXED, __HIP_MEMORY_SCOPE_AGENT); }
; __device__ __forceinline__ unsigned xb_add(unsigned* p, unsigned v) { return __hip_atomic_fetch_add(p, v, __ATOMIC_RELAXED, __HIP_MEMORY_SCOPE_AGENT); }
; #define XB_SPIN(cond, bar) do { unsigned _sp = 0; while (cond) { __builtin_amdgcn_s_sleep(1); \
;     if ((++_sp & 255u) == 0u) { if (xb_ld(&(bar)[XB_TMO])) break; if (_sp > XB_SPIN_CAP) { atomicAdd(&(bar)[XB_TMO], 1u); break; } } } } while (0)
; __device__ __forceinline__ void xcd_barrier(const XcdBarrier& b) {
;     ...
;     if (tid_from_wave(b.wave) == 0) {
;         unsigned* bar = b.bar;
;         __builtin_amdgcn_s_waitcnt(0);
;         unsigned nloc = b.st[0], nx = b.st[1];
;         if (nloc == 0u) { xcd_barrier_complete(bar, b.x, nloc, nx); b.st[0] = nloc; b.st[1] = nx; }
;         const unsigned old = xb_add(&bar[XB_XSUB(b.x)], 1u);
;         const unsigned gen = old / nloc;
;         if (old + 1u == (gen + 1u) * nloc) {
;             __builtin_amdgcn_fence(__ATOMIC_RELEASE, "agent");
;             asm volatile("s_waitcnt vmcnt(0)" ::: "memory");
;             const unsigned og = xb_add(&bar[XB_TOP], 1u);
;             const unsigned tg = og / nx;
;             if (og + 1u == (tg + 1u) * nx) xb_add(&bar[XB_TOPGEN], 1u);
;             else XB_SPIN(xb_ld(&bar[XB_TOPGEN]) == tg, bar);
;             __builtin_amdgcn_fence(__ATOMIC_ACQUIRE, "agent");
;             xb_add(&bar[XB_XGEN(b.x)], 1u);
;             asm volatile("s_waitcnt vmcnt(0)" ::: "memory");
;         } else {
;             XB_SPIN(xb_ld(&bar[XB_XGEN(b.x)]) == gen, bar);
;             __builtin_amdgcn_fence(__ATOMIC_ACQUIRE, "agent");
;             asm volatile("s_waitcnt vmcnt(0)" ::: "memory");
;         }
.LBB0_121:
	s_waitcnt lgkmcnt(0)
	v_readfirstlane_b32 s14, v2
	v_readfirstlane_b32 s15, v0
	s_lshl_b32 s12, s97, 8
	s_add_u32 s12, s92, s12
	s_addc_u32 s13, s93, 0
	v_mov_b32_e32 v0, 0x5400
	v_mov_b32_e32 v1, 1
	global_atomic_add v2, v0, v1, s[12:13] sc0
	s_add_i32 s17, s98, 1
	s_mul_i32 s18, s17, s14
	s_mul_i32 s19, s17, s15
	s_waitcnt vmcnt(0)
	buffer_inv sc1
	v_readfirstlane_b32 s16, v2
	s_add_i32 s16, s16, 1
	s_cmp_lg_u32 s16, s18
	s_cbranch_scc1 .Lxb_poll_0
	buffer_wbl2 sc1
	s_waitcnt vmcnt(0)
	v_mov_b32_e32 v0, 0x7400
	global_atomic_add v2, v0, v1, s[92:93] sc0
	s_waitcnt vmcnt(0)
	v_readfirstlane_b32 s16, v2
	s_add_i32 s16, s16, 1
	s_cmp_lg_u32 s16, s19
	s_cbranch_scc1 .Lxb_poll_0
	v_mov_b32_e32 v0, 0x7500
	global_atomic_add v0, v1, s[92:93]
	s_branch .Lxb_done_0
.Lxb_poll_0:
	v_mov_b32_e32 v0, 0x7500
	s_mov_b32 s20, 0
.Lxb_loop_0:
	global_load_dword v2, v0, s[92:93] sc1
	s_waitcnt vmcnt(0)
	v_readfirstlane_b32 s21, v2
	s_cmp_ge_u32 s21, s17
	s_cbranch_scc1 .Lxb_done_0
	s_sleep 1
	s_add_i32 s20, s20, 1
	s_and_b32 s16, s20, 0xff
	s_cmp_lg_u32 s16, 0
	s_cbranch_scc1 .Lxb_loop_0
	v_mov_b32_e32 v3, 0x4200
	global_load_dword v3, v3, s[92:93] sc1
	s_waitcnt vmcnt(0)
	v_readfirstlane_b32 s16, v3
	s_cmp_lg_u32 s16, 0
	s_cbranch_scc1 .Lxb_done_0
	s_cmp_lt_u32 s20, 0x40001
	s_cbranch_scc1 .Lxb_loop_0
	v_mov_b32_e32 v3, 0x4200
	global_atomic_add v3, v1, s[92:93]
